# out-proj epilogue: non-temporal hint on xin loads and X1 stores
# baseline (speedup 1.0000x reference)
.LBB0_728:
	s_add_i32 s13, s12, 0xffff8000
	s_and_b32 s13, s13, 0x8000
	s_add_i32 s23, s13, 0
	s_setprio 1
	s_and_b32 s13, s12, 0x8000
	s_add_i32 s13, s13, 0
	s_add_i32 s24, s13, s17
	v_lshl_add_u64 v[90:91], v[68:69], 0, s[10:11]
	s_mov_b32 m0, s24
	s_add_i32 s25, s13, s20
	global_load_lds_dwordx4 v[90:91], off
	v_lshl_add_u64 v[90:91], v[70:71], 0, s[10:11]
	s_mov_b32 m0, s25
	s_add_i32 s26, s13, s21
	global_load_lds_dwordx4 v[90:91], off
	v_lshl_add_u64 v[90:91], v[72:73], 0, s[10:11]
	s_mov_b32 m0, s26
	s_add_i32 s27, s13, s22
	global_load_lds_dwordx4 v[90:91], off
	v_lshl_add_u64 v[90:91], v[74:75], 0, s[10:11]
	s_mov_b32 m0, s27
	s_nop 0
	global_load_lds_dwordx4 v[90:91], off
	v_lshl_add_u64 v[90:91], v[76:77], 0, s[10:11]
	s_add_i32 m0, s24, 0x4000
	s_nop 0
	global_load_lds_dwordx4 v[90:91], off
	v_lshl_add_u64 v[90:91], v[78:79], 0, s[10:11]
	s_add_i32 m0, s25, 0x4000
	s_nop 0
	global_load_lds_dwordx4 v[90:91], off
	v_lshl_add_u64 v[90:91], v[80:81], 0, s[10:11]
	s_add_i32 m0, s26, 0x4000
	s_nop 0
	global_load_lds_dwordx4 v[90:91], off
	v_lshl_add_u64 v[90:91], v[82:83], 0, s[10:11]
	s_add_i32 m0, s27, 0x4000
	s_nop 0
	global_load_lds_dwordx4 v[90:91], off
	s_setprio 0
	v_add_u32_e32 v89, s23, v84
	v_add_u32_e32 v102, v89, v88
	ds_read_b128 v[90:93], v102
	v_add_u32_e32 v103, s23, v85
	v_add_u32_e32 v98, v103, v88
	ds_read_b128 v[94:97], v98 offset:16384
	ds_read_b128 v[98:101], v98 offset:20480
	s_add_u32 s10, s10, 0x80
	s_addc_u32 s11, s11, 0
	s_add_i32 s12, s12, 0x8000
	s_cmpk_lg_i32 s10, 0x780
	s_waitcnt lgkmcnt(0)
	v_mfma_f32_32x32x16_bf16 v[52:67], v[90:93], v[94:97], v[52:67]
	v_mfma_f32_32x32x16_bf16 v[20:35], v[90:93], v[98:101], v[20:35]
	ds_read_b128 v[90:93], v102 offset:4096
	v_add_u32_e32 v102, v89, v87
	s_waitcnt lgkmcnt(0)
	v_mfma_f32_32x32x16_bf16 v[36:51], v[90:93], v[94:97], v[36:51]
	v_mfma_f32_32x32x16_bf16 v[4:19], v[90:93], v[98:101], v[4:19]
	ds_read_b128 v[90:93], v102
	v_add_u32_e32 v98, v103, v87
	ds_read_b128 v[94:97], v98 offset:16384
	ds_read_b128 v[98:101], v98 offset:20480
	s_waitcnt lgkmcnt(0)
	v_mfma_f32_32x32x16_bf16 v[52:67], v[90:93], v[94:97], v[52:67]
	v_mfma_f32_32x32x16_bf16 v[20:35], v[90:93], v[98:101], v[20:35]
	ds_read_b128 v[90:93], v102 offset:4096
	v_add_u32_e32 v102, v89, v86
	v_add_u32_e32 v89, v89, v2
	s_waitcnt lgkmcnt(0)
	v_mfma_f32_32x32x16_bf16 v[36:51], v[90:93], v[94:97], v[36:51]
	v_mfma_f32_32x32x16_bf16 v[4:19], v[90:93], v[98:101], v[4:19]
	ds_read_b128 v[90:93], v102
	v_add_u32_e32 v98, v103, v86
	ds_read_b128 v[94:97], v98 offset:16384
	ds_read_b128 v[98:101], v98 offset:20480
	s_waitcnt lgkmcnt(0)
	v_mfma_f32_32x32x16_bf16 v[52:67], v[90:93], v[94:97], v[52:67]
	v_mfma_f32_32x32x16_bf16 v[20:35], v[90:93], v[98:101], v[20:35]
	ds_read_b128 v[90:93], v102 offset:4096
	s_waitcnt lgkmcnt(0)
	v_mfma_f32_32x32x16_bf16 v[36:51], v[90:93], v[94:97], v[36:51]
	v_mfma_f32_32x32x16_bf16 v[4:19], v[90:93], v[98:101], v[4:19]
	ds_read_b128 v[90:93], v89
	v_add_u32_e32 v98, v103, v2
	ds_read_b128 v[94:97], v98 offset:16384
	ds_read_b128 v[98:101], v98 offset:20480
	s_waitcnt lgkmcnt(0)
	v_mfma_f32_32x32x16_bf16 v[52:67], v[90:93], v[94:97], v[52:67]
	v_mfma_f32_32x32x16_bf16 v[20:35], v[90:93], v[98:101], v[20:35]
	ds_read_b128 v[90:93], v89 offset:4096
	s_waitcnt vmcnt(0) lgkmcnt(0)
	s_barrier
	v_mfma_f32_32x32x16_bf16 v[36:51], v[90:93], v[94:97], v[36:51]
	v_mfma_f32_32x32x16_bf16 v[4:19], v[90:93], v[98:101], v[4:19]
	s_cbranch_scc1 .LBB0_728
	s_setprio 1
	s_setprio 0
	s_add_i32 s10, s8, s35
	s_ashr_i32 s11, s10, 31
	s_lshr_b32 s11, s11, 19
	v_add_u32_e32 v84, s13, v84
	s_add_i32 s10, s10, s11
	v_add_u32_e32 v68, v84, v88
	s_ashr_i32 s10, s10, 13
	ds_read_b128 v[72:75], v68
	s_ashr_i32 s11, s10, 31
	s_add_u32 s10, s4, s10
	v_add_u32_e32 v108, s13, v85
	s_addc_u32 s11, s5, s11
	v_add_u32_e32 v69, v108, v88
	s_mulk_i32 s11, 0x6000
	s_mul_hi_u32 s12, s10, 0x6000
	ds_read_b128 v[88:91], v69 offset:16384
	ds_read_b128 v[114:117], v68 offset:4096
	ds_read_b128 v[118:121], v69 offset:20480
	s_add_i32 s12, s12, s11
	s_mulk_i32 s10, 0x6000
	s_add_u32 s10, s70, s10
	s_addc_u32 s11, s71, s12
	s_add_u32 s10, s10, 0x2000
	v_add_u32_e32 v68, v84, v87
	v_add_u32_e32 v76, v108, v87
	s_addc_u32 s11, s11, 0
	v_or_b32_e32 v142, s15, v112
	s_add_i32 s9, s9, s8
	v_lshrrev_b32_e32 v1, 3, v1
	s_waitcnt lgkmcnt(2)
	v_mfma_f32_32x32x16_bf16 v[52:67], v[72:75], v[88:91], v[52:67]
	ds_read_b128 v[122:125], v68
	ds_read_b128 v[68:71], v68 offset:4096
	v_add_u32_e32 v80, v108, v86
	v_and_or_b32 v136, v1, 4, s9
	v_lshlrev_b32_e32 v1, 2, v142
	v_ashrrev_i32_e32 v137, 31, v136
	v_lshlrev_b64 v[130:131], 12, v[136:137]
	v_or_b32_e32 v130, v130, v1
	s_waitcnt lgkmcnt(2)
	v_mfma_f32_32x32x16_bf16 v[20:35], v[72:75], v[118:121], v[20:35]
	ds_read_b128 v[100:103], v76 offset:16384
	ds_read_b128 v[72:75], v76 offset:20480
	v_add_u32_e32 v76, v84, v86
	v_add_u32_e32 v84, v84, v2
	v_add_u32_e32 v2, v108, v2
	ds_read_b128 v[92:95], v76
	ds_read_b128 v[76:79], v76 offset:4096
	ds_read_b128 v[104:107], v80 offset:16384
	ds_read_b128 v[80:83], v80 offset:20480
	ds_read_b128 v[96:99], v84
	ds_read_b128 v[84:87], v84 offset:4096
	v_mfma_f32_32x32x16_bf16 v[36:51], v[114:117], v[88:91], v[36:51]
	ds_read_b128 v[108:111], v2 offset:16384
	ds_read_b128 v[88:91], v2 offset:20480
	s_waitcnt lgkmcnt(0)
	s_barrier
	global_load_dword v126, v1, s[10:11]
	v_or_b32_e32 v2, s96, v142
	v_lshl_add_u64 v[112:113], v[2:3], 2, s[68:69]
	global_load_dword v2, v[112:113], off nt
	v_lshl_add_u64 v[112:113], s[0:1], 0, v[130:131]
	s_movk_i32 s8, 0x2000
	v_mfma_f32_32x32x16_bf16 v[4:19], v[114:117], v[118:121], v[4:19]
	v_add_co_u32_e32 v114, vcc, s8, v112
	s_mov_b32 s9, 0x9000
	s_nop 0
	v_addc_co_u32_e32 v115, vcc, 0, v113, vcc
	global_load_dword v132, v[112:113], off nt
	global_load_dword v133, v[114:115], off offset:-4096 nt
	v_add_co_u32_e32 v120, vcc, s91, v112
	s_mov_b32 s12, 0xb000
	s_nop 0
	v_addc_co_u32_e32 v121, vcc, 0, v113, vcc
	v_add_co_u32_e32 v118, vcc, s9, v112
	s_mov_b32 s13, 0x11000
	s_nop 0
	v_addc_co_u32_e32 v119, vcc, 0, v113, vcc
	v_add_co_u32_e32 v116, vcc, s12, v112
	v_mfma_f32_32x32x16_bf16 v[52:67], v[122:125], v[100:103], v[52:67]
	s_nop 0
	v_addc_co_u32_e32 v117, vcc, 0, v113, vcc
	global_load_dword v134, v[114:115], off nt
	global_load_dword v135, v[118:119], off offset:-4096 nt
	global_load_dword v137, v[118:119], off nt
	global_load_dword v138, v[116:117], off offset:-4096 nt
	global_load_dword v139, v[116:117], off nt
	global_load_dword v140, v[120:121], off nt
	s_mov_b32 s15, 0x13000
	s_mov_b32 s33, 0x1b000
	v_readlane_b32 s16, v253, 60
	v_readlane_b32 s18, v253, 62
	v_mfma_f32_32x32x16_bf16 v[20:35], v[122:125], v[72:75], v[20:35]
	v_add_co_u32_e32 v122, vcc, s13, v112
	v_readlane_b32 s19, v253, 63
	s_nop 0
	v_addc_co_u32_e32 v123, vcc, 0, v113, vcc
	global_load_dword v141, v[122:123], off offset:-4096 nt
	global_load_dword v143, v[122:123], off nt
	v_add_co_u32_e32 v124, vcc, s15, v112
	v_mfma_f32_32x32x16_bf16 v[52:67], v[92:95], v[104:107], v[52:67]
	s_nop 0
	v_addc_co_u32_e32 v125, vcc, 0, v113, vcc
	global_load_dword v144, v[124:125], off offset:-4096 nt
	global_load_dword v145, v[124:125], off nt
	v_lshl_add_u64 v[130:131], s[18:19], 0, v[130:131]
	s_mov_b32 s92, 0x18000
	v_readlane_b32 s17, v253, 61
	v_mfma_f32_32x32x16_bf16 v[52:67], v[96:99], v[108:111], v[52:67]
	v_readlane_b32 s20, v254, 0
	v_readlane_b32 s21, v254, 1
	v_readlane_b32 s22, v254, 2
	v_readlane_b32 s23, v254, 3
	v_readlane_b32 s24, v254, 4
	v_readlane_b32 s25, v254, 5
	v_readlane_b32 s26, v254, 6
	v_mfma_f32_32x32x16_bf16 v[36:51], v[68:71], v[100:103], v[36:51]
	v_readlane_b32 s27, v254, 7
	v_readlane_b32 s28, v254, 8
	v_readlane_b32 s29, v254, 9
	v_readlane_b32 s30, v254, 10
	v_readlane_b32 s31, v254, 11
	s_waitcnt vmcnt(13)
	v_add_f32_e32 v146, 1.0, v126
	v_add_co_u32_e32 v126, vcc, s86, v112
	s_waitcnt vmcnt(12)
	v_add_f32_e32 v52, v52, v2
	v_addc_co_u32_e32 v127, vcc, 0, v113, vcc
	global_load_dword v147, v[126:127], off offset:-4096 nt
	v_add_co_u32_e32 v128, vcc, s33, v112
	v_mul_f32_e32 v52, v146, v52
	s_nop 0
	v_addc_co_u32_e32 v129, vcc, 0, v113, vcc
	global_load_dword v148, v[126:127], off nt
	global_load_dword v149, v[128:129], off offset:-4096 nt
	global_load_dword v150, v[128:129], off nt
	s_waitcnt vmcnt(15)
	v_fmac_f32_e32 v52, 0x3fb504f3, v132
	global_store_dword v[130:131], v52, off nt
	s_waitcnt vmcnt(15)
	v_mul_f32_e32 v132, 0x3fb504f3, v133
	v_add_f32_e32 v52, v53, v2
	v_fmac_f32_e32 v132, v146, v52
	v_add_co_u32_e32 v52, vcc, s8, v130
	v_add_f32_e32 v54, v54, v2
	s_nop 0
	v_addc_co_u32_e32 v53, vcc, 0, v131, vcc
	global_store_dword v[52:53], v132, off offset:-4096 nt
	s_waitcnt vmcnt(15)
	v_mul_f32_e32 v132, 0x3fb504f3, v134
	v_fmac_f32_e32 v132, v146, v54
	global_store_dword v[52:53], v132, off nt
	v_add_f32_e32 v54, v55, v2
	s_waitcnt vmcnt(11)
	v_mul_f32_e32 v132, 0x3fb504f3, v140
	v_fmac_f32_e32 v132, v146, v54
	v_add_co_u32_e32 v54, vcc, s91, v130
	v_mul_f32_e32 v134, 0x3fb504f3, v135
	s_nop 0
	v_addc_co_u32_e32 v55, vcc, 0, v131, vcc
	v_add_f32_e32 v56, v56, v2
	global_store_dword v[54:55], v132, off nt
	v_fmac_f32_e32 v134, v146, v56
	v_add_co_u32_e32 v132, vcc, s9, v130
	v_mul_f32_e32 v56, 0x3fb504f3, v137
	v_add_f32_e32 v57, v57, v2
	v_addc_co_u32_e32 v133, vcc, 0, v131, vcc
	v_fmac_f32_e32 v56, v146, v57
	global_store_dword v[132:133], v134, off offset:-4096 nt
	global_store_dword v[132:133], v56, off nt
	v_mul_f32_e32 v134, 0x3fb504f3, v138
	v_add_f32_e32 v56, v58, v2
	v_fmac_f32_e32 v134, v146, v56
	v_add_co_u32_e32 v56, vcc, s12, v130
	v_mul_f32_e32 v58, 0x3fb504f3, v139
	v_add_f32_e32 v59, v59, v2
	v_addc_co_u32_e32 v57, vcc, 0, v131, vcc
	v_fmac_f32_e32 v58, v146, v59
	global_store_dword v[56:57], v134, off offset:-4096 nt
	global_store_dword v[56:57], v58, off nt
	s_waitcnt vmcnt(15)
	v_mul_f32_e32 v134, 0x3fb504f3, v141
	v_add_f32_e32 v58, v60, v2
	v_fmac_f32_e32 v134, v146, v58
	v_add_co_u32_e32 v58, vcc, s13, v130
	s_waitcnt vmcnt(14)
	v_mul_f32_e32 v60, 0x3fb504f3, v143
	v_add_f32_e32 v61, v61, v2
	v_addc_co_u32_e32 v59, vcc, 0, v131, vcc
	v_fmac_f32_e32 v60, v146, v61
	global_store_dword v[58:59], v134, off offset:-4096 nt
	global_store_dword v[58:59], v60, off nt
	s_waitcnt vmcnt(15)
	v_mul_f32_e32 v134, 0x3fb504f3, v144
	v_add_f32_e32 v60, v62, v2
	v_fmac_f32_e32 v134, v146, v60
	v_add_co_u32_e32 v60, vcc, s15, v130
	s_waitcnt vmcnt(14)
	v_mul_f32_e32 v62, 0x3fb504f3, v145
	v_add_f32_e32 v63, v63, v2
	v_addc_co_u32_e32 v61, vcc, 0, v131, vcc
	v_fmac_f32_e32 v62, v146, v63
	global_store_dword v[60:61], v134, off offset:-4096 nt
	global_store_dword v[60:61], v62, off nt
	v_add_f32_e32 v63, v64, v2
	v_add_co_u32_e32 v134, vcc, s86, v130
	s_waitcnt vmcnt(15)
	v_mul_f32_e32 v62, 0x3fb504f3, v147
	v_fmac_f32_e32 v62, v146, v63
	v_addc_co_u32_e32 v135, vcc, 0, v131, vcc
	global_store_dword v[134:135], v62, off offset:-4096 nt
	s_waitcnt vmcnt(15)
	v_mul_f32_e32 v62, 0x3fb504f3, v148
	v_add_f32_e32 v63, v65, v2
	v_fmac_f32_e32 v62, v146, v63
	global_store_dword v[134:135], v62, off nt
	s_waitcnt vmcnt(15)
	v_mul_f32_e32 v62, 0x3fb504f3, v149
	v_add_f32_e32 v63, v66, v2
	v_add_co_u32_e32 v64, vcc, s33, v130
	v_fmac_f32_e32 v62, v146, v63
	s_nop 0
	v_addc_co_u32_e32 v65, vcc, 0, v131, vcc
	global_store_dword v[64:65], v62, off offset:-4096 nt
	s_waitcnt vmcnt(15)
	v_mul_f32_e32 v62, 0x3fb504f3, v150
	v_add_f32_e32 v63, v67, v2
	v_fmac_f32_e32 v62, v146, v63
	global_store_dword v[64:65], v62, off nt
	v_or_b32_e32 v62, 32, v136
	v_ashrrev_i32_e32 v63, 31, v62
	v_lshlrev_b64 v[144:145], 12, v[62:63]
	v_or_b32_e32 v144, v144, v1
	v_lshl_add_u64 v[62:63], s[0:1], 0, v[144:145]
	v_add_co_u32_e32 v66, vcc, s8, v62
	v_mfma_f32_32x32x16_bf16 v[36:51], v[76:79], v[104:107], v[36:51]
	s_nop 0
	v_addc_co_u32_e32 v67, vcc, 0, v63, vcc
	global_load_dword v143, v[62:63], off nt
	global_load_dword v147, v[66:67], off offset:-4096 nt
	v_add_co_u32_e32 v140, vcc, s91, v62
	v_lshl_add_u64 v[102:103], s[18:19], 0, v[144:145]
	s_nop 0
	v_addc_co_u32_e32 v141, vcc, 0, v63, vcc
	v_add_co_u32_e32 v138, vcc, s9, v62
	v_mfma_f32_32x32x16_bf16 v[36:51], v[84:87], v[108:111], v[36:51]
	s_nop 0
	v_addc_co_u32_e32 v139, vcc, 0, v63, vcc
	v_add_co_u32_e32 v136, vcc, s12, v62
	v_or_b32_e32 v1, 0x80, v1
	s_nop 0
	v_addc_co_u32_e32 v137, vcc, 0, v63, vcc
	global_load_dword v148, v[66:67], off nt
	global_load_dword v149, v[138:139], off offset:-4096 nt
	global_load_dword v150, v[138:139], off nt
	global_load_dword v151, v[136:137], off offset:-4096 nt
	global_load_dword v152, v[136:137], off nt
	global_load_dword v153, v[140:141], off nt
	v_add_co_u32_e32 v100, vcc, s13, v62
	v_add_f32_e32 v36, v36, v2
	s_nop 0
	v_addc_co_u32_e32 v101, vcc, 0, v63, vcc
	global_load_dword v154, v[100:101], off offset:-4096 nt
	global_load_dword v155, v[100:101], off nt
	v_add_co_u32_e32 v104, vcc, s15, v62
	v_add_f32_e32 v38, v38, v2
	s_nop 0
	v_addc_co_u32_e32 v105, vcc, 0, v63, vcc
	global_load_dword v156, v[104:105], off offset:-4096 nt
	global_load_dword v157, v[104:105], off nt
	v_add_co_u32_e32 v106, vcc, s86, v62
	v_add_f32_e32 v40, v40, v2
	s_nop 0
	v_addc_co_u32_e32 v107, vcc, 0, v63, vcc
	global_load_dword v158, v[106:107], off offset:-4096 nt
	v_add_co_u32_e32 v108, vcc, s33, v62
	v_add_f32_e32 v41, v41, v2
	s_nop 0
	v_addc_co_u32_e32 v109, vcc, 0, v63, vcc
	global_load_dword v159, v[106:107], off nt
	global_load_dword v160, v[108:109], off offset:-4096 nt
	global_load_dword v161, v[108:109], off nt
	v_add_f32_e32 v43, v43, v2
	v_add_f32_e32 v45, v45, v2
	v_add_f32_e32 v47, v47, v2
	v_add_f32_e32 v49, v49, v2
	v_mfma_f32_32x32x16_bf16 v[20:35], v[92:95], v[80:83], v[20:35]
	s_waitcnt vmcnt(15)
	v_mul_f32_e32 v110, 0x3fb504f3, v143
	v_fmac_f32_e32 v110, v146, v36
	global_store_dword v[102:103], v110, off nt
	s_waitcnt vmcnt(15)
	v_mul_f32_e32 v110, 0x3fb504f3, v147
	v_add_f32_e32 v36, v37, v2
	v_fmac_f32_e32 v110, v146, v36
	v_add_co_u32_e32 v36, vcc, s8, v102
	s_movk_i32 s8, 0x1000
	s_nop 0
	v_addc_co_u32_e32 v37, vcc, 0, v103, vcc
	global_store_dword v[36:37], v110, off offset:-4096 nt
	s_waitcnt vmcnt(15)
	v_mul_f32_e32 v110, 0x3fb504f3, v148
	v_fmac_f32_e32 v110, v146, v38
	global_store_dword v[36:37], v110, off nt
	v_add_f32_e32 v38, v39, v2
	s_waitcnt vmcnt(15)
	v_mul_f32_e32 v143, 0x3fb504f3, v149
	s_waitcnt vmcnt(11)
	v_mul_f32_e32 v110, 0x3fb504f3, v153
	v_fmac_f32_e32 v110, v146, v38
	v_add_co_u32_e32 v38, vcc, s91, v102
	v_fmac_f32_e32 v143, v146, v40
	s_nop 0
	v_addc_co_u32_e32 v39, vcc, 0, v103, vcc
	global_store_dword v[38:39], v110, off nt
	v_add_co_u32_e32 v110, vcc, s9, v102
	v_mul_f32_e32 v40, 0x3fb504f3, v150
	s_nop 0
	v_addc_co_u32_e32 v111, vcc, 0, v103, vcc
	v_fmac_f32_e32 v40, v146, v41
	global_store_dword v[110:111], v143, off offset:-4096 nt
	global_store_dword v[110:111], v40, off nt
	v_mul_f32_e32 v143, 0x3fb504f3, v151
	v_add_f32_e32 v40, v42, v2
	v_fmac_f32_e32 v143, v146, v40
	v_add_co_u32_e32 v40, vcc, s12, v102
	v_mul_f32_e32 v42, 0x3fb504f3, v152
	s_nop 0
	v_addc_co_u32_e32 v41, vcc, 0, v103, vcc
	v_fmac_f32_e32 v42, v146, v43
	global_store_dword v[40:41], v143, off offset:-4096 nt
	global_store_dword v[40:41], v42, off nt
	s_waitcnt vmcnt(15)
	v_mul_f32_e32 v143, 0x3fb504f3, v154
	v_add_f32_e32 v42, v44, v2
	v_fmac_f32_e32 v143, v146, v42
	v_add_co_u32_e32 v42, vcc, s13, v102
	s_waitcnt vmcnt(14)
	v_mul_f32_e32 v44, 0x3fb504f3, v155
	v_addc_co_u32_e32 v43, vcc, 0, v103, vcc
	v_fmac_f32_e32 v44, v146, v45
	global_store_dword v[42:43], v143, off offset:-4096 nt
	global_store_dword v[42:43], v44, off nt
	s_waitcnt vmcnt(15)
	v_mul_f32_e32 v143, 0x3fb504f3, v156
	v_add_f32_e32 v44, v46, v2
	v_fmac_f32_e32 v143, v146, v44
	v_add_co_u32_e32 v44, vcc, s15, v102
	s_waitcnt vmcnt(14)
	v_mul_f32_e32 v46, 0x3fb504f3, v157
	v_addc_co_u32_e32 v45, vcc, 0, v103, vcc
	v_fmac_f32_e32 v46, v146, v47
	global_store_dword v[44:45], v143, off offset:-4096 nt
	global_store_dword v[44:45], v46, off nt
	s_waitcnt vmcnt(15)
	v_mul_f32_e32 v143, 0x3fb504f3, v158
	v_add_f32_e32 v46, v48, v2
	v_fmac_f32_e32 v143, v146, v46
	v_add_co_u32_e32 v46, vcc, s86, v102
	s_waitcnt vmcnt(14)
	v_mul_f32_e32 v48, 0x3fb504f3, v159
	v_addc_co_u32_e32 v47, vcc, 0, v103, vcc
	v_fmac_f32_e32 v48, v146, v49
	global_store_dword v[46:47], v143, off offset:-4096 nt
	global_store_dword v[46:47], v48, off nt
	s_waitcnt vmcnt(15)
	v_mul_f32_e32 v143, 0x3fb504f3, v160
	v_add_f32_e32 v48, v50, v2
	v_fmac_f32_e32 v143, v146, v48
	v_add_co_u32_e32 v48, vcc, s33, v102
	s_waitcnt vmcnt(14)
	v_mul_f32_e32 v50, 0x3fb504f3, v161
	v_add_f32_e32 v2, v51, v2
	v_addc_co_u32_e32 v49, vcc, 0, v103, vcc
	v_fmac_f32_e32 v50, v146, v2
	global_store_dword v[48:49], v143, off offset:-4096 nt
	global_store_dword v[48:49], v50, off nt
	v_add_u32_e32 v2, s96, v142
	global_load_dword v1, v1, s[10:11]
	v_lshl_add_u64 v[50:51], v[2:3], 2, s[68:69]
	global_load_dword v2, v[50:51], off offset:128 nt
	global_load_dword v142, v[112:113], off offset:128 nt
	v_add_co_u32_e32 v50, vcc, s8, v112
	s_mov_b32 s9, 0x8000
	s_nop 0
	v_addc_co_u32_e32 v51, vcc, 0, v113, vcc
	global_load_dword v143, v[50:51], off offset:128 nt
	global_load_dword v144, v[114:115], off offset:128 nt
	v_add_co_u32_e32 v50, vcc, s9, v112
	global_load_dword v120, v[120:121], off offset:128 nt
	s_nop 0
	v_addc_co_u32_e32 v51, vcc, 0, v113, vcc
	global_load_dword v121, v[50:51], off offset:128 nt
	s_nop 0
	global_load_dword v118, v[118:119], off offset:128 nt
	s_mov_b32 s12, 0xa000
	v_add_co_u32_e32 v50, vcc, s12, v112
	s_mov_b32 s10, 0x10000
	s_nop 0
	v_addc_co_u32_e32 v51, vcc, 0, v113, vcc
	global_load_dword v119, v[50:51], off offset:128 nt
	s_mov_b32 s11, 0x12000
	global_load_dword v116, v[116:117], off offset:128 nt
	v_add_co_u32_e32 v50, vcc, s10, v112
	s_mov_b32 s13, 0x18000
	s_nop 0
	v_addc_co_u32_e32 v51, vcc, 0, v113, vcc
	global_load_dword v117, v[50:51], off offset:128 nt
	v_add_co_u32_e32 v50, vcc, s11, v112
	v_mfma_f32_32x32x16_bf16 v[20:35], v[96:99], v[88:91], v[20:35]
	s_nop 0
	v_addc_co_u32_e32 v51, vcc, 0, v113, vcc
	global_load_dword v122, v[122:123], off offset:128 nt
	s_nop 0
	global_load_dword v123, v[50:51], off offset:128 nt
	v_add_co_u32_e32 v50, vcc, s13, v112
	global_load_dword v124, v[124:125], off offset:128 nt
	s_nop 0
	v_addc_co_u32_e32 v51, vcc, 0, v113, vcc
	global_load_dword v125, v[50:51], off offset:128 nt
	v_add_co_u32_e32 v92, vcc, s93, v112
	v_mfma_f32_32x32x16_bf16 v[4:19], v[68:71], v[72:75], v[4:19]
	s_nop 0
	v_addc_co_u32_e32 v93, vcc, 0, v113, vcc
	global_load_dword v126, v[126:127], off offset:128 nt
	s_nop 0
	global_load_dword v127, v[92:93], off offset:128 nt
	v_add_co_u32_e32 v50, vcc, s8, v130
	global_load_dword v128, v[128:129], off offset:128 nt
	s_nop 0
	v_addc_co_u32_e32 v51, vcc, 0, v131, vcc
	v_add_co_u32_e32 v92, vcc, s9, v130
	v_mfma_f32_32x32x16_bf16 v[4:19], v[76:79], v[80:83], v[4:19]
	s_nop 0
	v_addc_co_u32_e32 v93, vcc, 0, v131, vcc
	v_add_co_u32_e32 v94, vcc, s12, v130
	s_waitcnt vmcnt(17)
	v_add_f32_e32 v1, 1.0, v1
	s_waitcnt vmcnt(16)
	v_add_f32_e32 v20, v20, v2
	v_mul_f32_e32 v20, v1, v20
	s_waitcnt vmcnt(15)
	v_fmac_f32_e32 v20, 0x3fb504f3, v142
	global_store_dword v[130:131], v20, off offset:128 nt
	v_add_f32_e32 v21, v21, v2
	v_addc_co_u32_e32 v95, vcc, 0, v131, vcc
	s_waitcnt vmcnt(15)
	v_mul_f32_e32 v20, 0x3fb504f3, v143
	v_fmac_f32_e32 v20, v1, v21
	global_store_dword v[50:51], v20, off offset:128 nt
	s_waitcnt vmcnt(15)
	v_mul_f32_e32 v20, 0x3fb504f3, v144
	v_add_f32_e32 v21, v22, v2
	v_fmac_f32_e32 v20, v1, v21
	global_store_dword v[52:53], v20, off offset:128 nt
	s_waitcnt vmcnt(15)
	v_mul_f32_e32 v20, 0x3fb504f3, v120
	v_add_f32_e32 v21, v23, v2
	v_fmac_f32_e32 v20, v1, v21
	global_store_dword v[54:55], v20, off offset:128 nt
	s_waitcnt vmcnt(15)
	v_mul_f32_e32 v20, 0x3fb504f3, v121
	v_add_f32_e32 v21, v24, v2
	v_fmac_f32_e32 v20, v1, v21
	global_store_dword v[92:93], v20, off offset:128 nt
	s_waitcnt vmcnt(15)
	v_mul_f32_e32 v20, 0x3fb504f3, v118
	v_add_f32_e32 v21, v25, v2
	v_fmac_f32_e32 v20, v1, v21
	global_store_dword v[132:133], v20, off offset:128 nt
	s_waitcnt vmcnt(15)
	v_mul_f32_e32 v20, 0x3fb504f3, v119
	v_add_f32_e32 v21, v26, v2
	v_fmac_f32_e32 v20, v1, v21
	global_store_dword v[94:95], v20, off offset:128 nt
	s_waitcnt vmcnt(15)
	v_mul_f32_e32 v20, 0x3fb504f3, v116
	v_add_f32_e32 v21, v27, v2
	v_fmac_f32_e32 v20, v1, v21
	v_add_co_u32_e32 v96, vcc, s10, v130
	global_store_dword v[56:57], v20, off offset:128 nt
	s_waitcnt vmcnt(15)
	v_mul_f32_e32 v20, 0x3fb504f3, v117
	v_add_f32_e32 v21, v28, v2
	v_addc_co_u32_e32 v97, vcc, 0, v131, vcc
	v_fmac_f32_e32 v20, v1, v21
	global_store_dword v[96:97], v20, off offset:128 nt
	s_waitcnt vmcnt(15)
	v_mul_f32_e32 v20, 0x3fb504f3, v122
	v_add_f32_e32 v21, v29, v2
	v_fmac_f32_e32 v20, v1, v21
	v_add_co_u32_e32 v98, vcc, s11, v130
	global_store_dword v[58:59], v20, off offset:128 nt
	s_waitcnt vmcnt(15)
	v_mul_f32_e32 v20, 0x3fb504f3, v123
	v_add_f32_e32 v21, v30, v2
	v_addc_co_u32_e32 v99, vcc, 0, v131, vcc
	v_fmac_f32_e32 v20, v1, v21
	global_store_dword v[98:99], v20, off offset:128 nt
	s_waitcnt vmcnt(15)
	v_mul_f32_e32 v20, 0x3fb504f3, v124
	v_add_f32_e32 v21, v31, v2
	v_fmac_f32_e32 v20, v1, v21
	v_add_co_u32_e32 v112, vcc, s13, v130
	global_store_dword v[60:61], v20, off offset:128 nt
	s_waitcnt vmcnt(15)
	v_mul_f32_e32 v20, 0x3fb504f3, v125
	v_add_f32_e32 v21, v32, v2
	v_addc_co_u32_e32 v113, vcc, 0, v131, vcc
	v_fmac_f32_e32 v20, v1, v21
	global_store_dword v[112:113], v20, off offset:128 nt
	s_waitcnt vmcnt(15)
	v_mul_f32_e32 v20, 0x3fb504f3, v126
	v_add_f32_e32 v21, v33, v2
	v_fmac_f32_e32 v20, v1, v21
	v_add_co_u32_e32 v114, vcc, s93, v130
	global_store_dword v[134:135], v20, off offset:128 nt
	s_waitcnt vmcnt(15)
	v_mul_f32_e32 v20, 0x3fb504f3, v127
	v_add_f32_e32 v21, v34, v2
	v_addc_co_u32_e32 v115, vcc, 0, v131, vcc
	v_fmac_f32_e32 v20, v1, v21
	global_store_dword v[114:115], v20, off offset:128 nt
	s_waitcnt vmcnt(15)
	v_mul_f32_e32 v20, 0x3fb504f3, v128
	v_add_f32_e32 v21, v35, v2
	v_fmac_f32_e32 v20, v1, v21
	global_store_dword v[64:65], v20, off offset:128 nt
	global_load_dword v34, v[62:63], off offset:128 nt
	v_add_co_u32_e32 v20, vcc, s8, v62
	v_mfma_f32_32x32x16_bf16 v[4:19], v[84:87], v[88:91], v[4:19]
	s_nop 0
	v_addc_co_u32_e32 v21, vcc, 0, v63, vcc
	global_load_dword v35, v[20:21], off offset:128 nt
	global_load_dword v50, v[66:67], off offset:128 nt
	global_load_dword v51, v[140:141], off offset:128 nt
	global_load_dword v55, v[136:137], off offset:128 nt
	v_add_co_u32_e32 v20, vcc, s9, v62
	global_load_dword v53, v[138:139], off offset:128 nt
	s_nop 0
	v_addc_co_u32_e32 v21, vcc, 0, v63, vcc
	global_load_dword v52, v[20:21], off offset:128 nt
	v_add_co_u32_e32 v20, vcc, s12, v62
	v_add_f32_e32 v4, v4, v2
	s_nop 0
	v_addc_co_u32_e32 v21, vcc, 0, v63, vcc
	global_load_dword v54, v[20:21], off offset:128 nt
	v_add_co_u32_e32 v20, vcc, s10, v62
	v_add_f32_e32 v5, v5, v2
	s_nop 0
	v_addc_co_u32_e32 v21, vcc, 0, v63, vcc
	global_load_dword v56, v[20:21], off offset:128 nt
	global_load_dword v57, v[100:101], off offset:128 nt
	v_add_co_u32_e32 v20, vcc, s11, v62
	global_load_dword v59, v[104:105], off offset:128 nt
	s_nop 0
	v_addc_co_u32_e32 v21, vcc, 0, v63, vcc
	global_load_dword v58, v[20:21], off offset:128 nt
	v_add_co_u32_e32 v20, vcc, s13, v62
	s_waitcnt vmcnt(11)
	v_mul_f32_e32 v34, 0x3fb504f3, v34
	v_addc_co_u32_e32 v21, vcc, 0, v63, vcc
	global_load_dword v60, v[20:21], off offset:128 nt
	global_load_dword v61, v[106:107], off offset:128 nt
	v_add_co_u32_e32 v22, vcc, s93, v62
	v_fmac_f32_e32 v34, v1, v4
	s_nop 0
	v_addc_co_u32_e32 v23, vcc, 0, v63, vcc
	global_load_dword v62, v[108:109], off offset:128 nt
	global_load_dword v63, v[22:23], off offset:128 nt
	v_add_co_u32_e32 v20, vcc, s8, v102
	s_waitcnt vmcnt(14)
	v_mul_f32_e32 v4, 0x3fb504f3, v35
	v_addc_co_u32_e32 v21, vcc, 0, v103, vcc
	v_fmac_f32_e32 v4, v1, v5
	global_store_dword v[20:21], v4, off offset:128 nt
	s_waitcnt vmcnt(14)
	v_mul_f32_e32 v4, 0x3fb504f3, v50
	v_add_f32_e32 v5, v6, v2
	v_fmac_f32_e32 v4, v1, v5
	global_store_dword v[36:37], v4, off offset:128 nt
	s_waitcnt vmcnt(14)
	v_mul_f32_e32 v4, 0x3fb504f3, v51
	v_add_f32_e32 v5, v7, v2
	v_fmac_f32_e32 v4, v1, v5
	v_add_co_u32_e32 v22, vcc, s9, v102
	global_store_dword v[38:39], v4, off offset:128 nt
	s_waitcnt vmcnt(12)
	v_mul_f32_e32 v4, 0x3fb504f3, v52
	v_add_f32_e32 v5, v8, v2
	v_addc_co_u32_e32 v23, vcc, 0, v103, vcc
	v_fmac_f32_e32 v4, v1, v5
	global_store_dword v[22:23], v4, off offset:128 nt
	v_mul_f32_e32 v4, 0x3fb504f3, v53
	v_add_f32_e32 v5, v9, v2
	v_fmac_f32_e32 v4, v1, v5
	v_add_co_u32_e32 v24, vcc, s12, v102
	global_store_dword v[110:111], v4, off offset:128 nt
	s_waitcnt vmcnt(13)
	v_mul_f32_e32 v4, 0x3fb504f3, v54
	v_add_f32_e32 v5, v10, v2
	v_addc_co_u32_e32 v25, vcc, 0, v103, vcc
	v_fmac_f32_e32 v4, v1, v5
	global_store_dword v[24:25], v4, off offset:128 nt
	v_mul_f32_e32 v4, 0x3fb504f3, v55
	v_add_f32_e32 v5, v11, v2
	v_fmac_f32_e32 v4, v1, v5
	v_add_co_u32_e32 v26, vcc, s10, v102
	global_store_dword v[40:41], v4, off offset:128 nt
	s_waitcnt vmcnt(14)
	v_mul_f32_e32 v4, 0x3fb504f3, v56
	v_add_f32_e32 v5, v12, v2
	v_addc_co_u32_e32 v27, vcc, 0, v103, vcc
	v_fmac_f32_e32 v4, v1, v5
	global_store_dword v[26:27], v4, off offset:128 nt
	s_waitcnt vmcnt(14)
	v_mul_f32_e32 v4, 0x3fb504f3, v57
	v_add_f32_e32 v5, v13, v2
	v_fmac_f32_e32 v4, v1, v5
	v_add_co_u32_e32 v28, vcc, s11, v102
	global_store_dword v[42:43], v4, off offset:128 nt
	s_waitcnt vmcnt(13)
	v_mul_f32_e32 v4, 0x3fb504f3, v58
	v_add_f32_e32 v5, v14, v2
	v_addc_co_u32_e32 v29, vcc, 0, v103, vcc
	v_fmac_f32_e32 v4, v1, v5
	global_store_dword v[28:29], v4, off offset:128 nt
	v_mul_f32_e32 v4, 0x3fb504f3, v59
	v_add_f32_e32 v5, v15, v2
	v_fmac_f32_e32 v4, v1, v5
	v_add_co_u32_e32 v30, vcc, s13, v102
	global_store_dword v[44:45], v4, off offset:128 nt
	v_add_f32_e32 v5, v16, v2
	v_addc_co_u32_e32 v31, vcc, 0, v103, vcc
	v_add_co_u32_e32 v32, vcc, s93, v102
	global_store_dword v[102:103], v34, off offset:128 nt
	s_nop 0
	v_addc_co_u32_e32 v33, vcc, 0, v103, vcc
	s_waitcnt vmcnt(15)
	v_mul_f32_e32 v4, 0x3fb504f3, v60
	v_fmac_f32_e32 v4, v1, v5
	global_store_dword v[30:31], v4, off offset:128 nt
	s_waitcnt vmcnt(15)
	v_mul_f32_e32 v4, 0x3fb504f3, v61
	v_add_f32_e32 v5, v17, v2
	v_fmac_f32_e32 v4, v1, v5
	global_store_dword v[46:47], v4, off offset:128 nt
	s_waitcnt vmcnt(14)
	v_mul_f32_e32 v4, 0x3fb504f3, v63
	v_add_f32_e32 v5, v18, v2
	v_fmac_f32_e32 v4, v1, v5
	global_store_dword v[32:33], v4, off offset:128 nt
	v_mul_f32_e32 v4, 0x3fb504f3, v62
	v_add_f32_e32 v2, v19, v2
	v_fmac_f32_e32 v4, v1, v2
	global_store_dword v[48:49], v4, off offset:128 nt
	v_mov_b32_e32 v1, s36
	ds_read_b32 v2, v1
	s_load_dword s8, s[94:95], 0x0
	ds_read_b32 v1, v1
	s_waitcnt lgkmcnt(0)
	v_readfirstlane_b32 s10, v2
	s_ashr_i32 s9, s8, 31
	s_lshr_b32 s9, s9, 29
	s_add_i32 s9, s8, s9
	s_ashr_i32 s9, s9, 3
	s_cmp_eq_u32 s10, 0
	s_cselect_b32 s8, s8, s9
	v_cmp_eq_u32_e32 vcc, 0, v1
	s_add_i32 s2, s8, s2
	s_nop 0
	v_cndmask_b32_e32 v1, v207, v208, vcc
	v_cmp_ge_i32_e32 vcc, s2, v1
	s_cbranch_vccz .LBB0_725
